# MLA attention: next key tile's global loads issued at the top of the tile loop (dedicated destination registers), 3-4 deep LDS fragment prefetch
# speedup vs baseline: 1.0032x; 1.0032x over previous
.LBB0_1038:
	s_bitcmp1_b32 s22, 0
	s_cselect_b32 s23, 0xac00, 0
	s_add_i32 s23, s23, 0
	v_lshl_add_u64 v[4:5], s[26:27], 0, v[208:209]
	v_lshl_add_u64 v[6:7], s[26:27], 0, v[216:217]
	v_lshl_add_u64 v[8:9], s[26:27], 0, v[214:215]
	v_lshl_add_u64 v[10:11], s[26:27], 0, v[210:211]
	v_lshl_add_u64 v[16:17], s[26:27], 0, v[212:213]
	s_nop 0
	global_load_dwordx4 v[150:153], v[4:5], off
	global_load_dwordx4 v[146:149], v[6:7], off
	global_load_dwordx4 v[12:15], v[8:9], off
	global_load_dwordx4 v[248:251], v[10:11], off
	global_load_dwordx4 v[252:255], v[16:17], off
	v_add3_u32 v2, s23, v228, v154
	ds_read_b128 v[4:7], v2
	ds_read_b128 v[8:11], v2 offset:32
	ds_read_b128 v[238:241], v2 offset:64
	s_waitcnt lgkmcnt(2)
	v_mfma_f32_32x32x16_bf16 v[82:97], v[4:7], v[142:145], 0
	ds_read_b128 v[4:7], v2 offset:96
	s_waitcnt lgkmcnt(2)
	v_mfma_f32_32x32x16_bf16 v[82:97], v[8:11], v[138:141], v[82:97]
	ds_read_b128 v[8:11], v2 offset:128
	s_waitcnt lgkmcnt(2)
	v_mfma_f32_32x32x16_bf16 v[82:97], v[238:241], v[134:137], v[82:97]
	ds_read_b128 v[238:241], v2 offset:160
	s_waitcnt lgkmcnt(2)
	v_mfma_f32_32x32x16_bf16 v[82:97], v[4:7], v[130:133], v[82:97]
	ds_read_b128 v[4:7], v2 offset:192
	s_waitcnt lgkmcnt(2)
	v_mfma_f32_32x32x16_bf16 v[82:97], v[8:11], v[126:129], v[82:97]
	ds_read_b128 v[8:11], v2 offset:224
	s_waitcnt lgkmcnt(2)
	v_mfma_f32_32x32x16_bf16 v[82:97], v[238:241], v[122:125], v[82:97]
	ds_read_b128 v[238:241], v2 offset:256
	s_waitcnt lgkmcnt(2)
	v_mfma_f32_32x32x16_bf16 v[82:97], v[4:7], v[118:121], v[82:97]
	ds_read_b128 v[4:7], v2 offset:288
	s_waitcnt lgkmcnt(2)
	v_mfma_f32_32x32x16_bf16 v[82:97], v[8:11], v[114:117], v[82:97]
	ds_read_b128 v[8:11], v2 offset:320
	s_waitcnt lgkmcnt(2)
	v_mfma_f32_32x32x16_bf16 v[82:97], v[238:241], v[110:113], v[82:97]
	ds_read_b128 v[238:241], v2 offset:352
	s_waitcnt lgkmcnt(2)
	v_mfma_f32_32x32x16_bf16 v[82:97], v[4:7], v[106:109], v[82:97]
	s_waitcnt lgkmcnt(1)
	v_mfma_f32_32x32x16_bf16 v[82:97], v[8:11], v[102:105], v[82:97]
	s_waitcnt lgkmcnt(0)
	v_mov_b32_e32 v2, v236
	v_max_f32_e32 v16, v2, v2
	v_mfma_f32_32x32x16_bf16 v[82:97], v[238:241], v[98:101], v[82:97]
	s_nop 11
	v_max3_f32 v17, v82, s19, v83
	v_max3_f32 v17, v17, v84, v85
	v_max3_f32 v17, v17, v86, v87
	v_max3_f32 v17, v17, v88, v89
	v_max3_f32 v17, v17, v90, v91
	v_max3_f32 v17, v17, v92, v93
	v_max3_f32 v17, v17, v94, v95
	v_max3_f32 v17, v17, v96, v97
	v_mov_b32_e32 v236, v17
	s_nop 1
	v_permlane32_swap_b32_e32 v17, v236
	v_mul_f32_e32 v17, 0x3dd53b95, v17
	v_max_f32_e32 v236, v16, v17
	v_fma_f32 v16, v82, s20, -v236
	v_fma_f32 v17, v83, s20, -v236
	v_fma_f32 v241, v94, s20, -v236
	v_exp_f32_e32 v94, v16
	v_fma_f32 v82, v84, s20, -v236
	v_fma_f32 v243, v96, s20, -v236
	v_exp_f32_e32 v96, v17
	v_fma_f32 v83, v85, s20, -v236
	v_fma_f32 v239, v92, s20, -v236
	v_exp_f32_e32 v92, v82
	v_fma_f32 v84, v86, s20, -v236
	v_fma_f32 v242, v95, s20, -v236
	v_exp_f32_e32 v95, v83
	v_fma_f32 v85, v87, s20, -v236
	v_fma_f32 v86, v88, s20, -v236
	v_fma_f32 v88, v90, s20, -v236
	v_exp_f32_e32 v90, v84
	v_add_f32_e32 v16, 0, v94
	v_fma_f32 v240, v93, s20, -v236
	v_exp_f32_e32 v93, v85
	v_add_f32_e32 v16, v96, v16
	v_fma_f32 v87, v89, s20, -v236
	v_exp_f32_e32 v89, v86
	v_add_f32_e32 v16, v92, v16
	v_fma_f32 v238, v91, s20, -v236
	v_exp_f32_e32 v91, v87
	v_add_f32_e32 v16, v95, v16
	v_exp_f32_e32 v84, v88
	v_add_f32_e32 v16, v90, v16
	v_exp_f32_e32 v87, v238
	v_add_f32_e32 v16, v93, v16
	v_exp_f32_e32 v82, v239
	v_add_f32_e32 v16, v89, v16
	v_exp_f32_e32 v85, v240
	v_add_f32_e32 v16, v91, v16
	v_exp_f32_e32 v17, v241
	v_add_f32_e32 v16, v84, v16
	v_exp_f32_e32 v83, v242
	v_add_f32_e32 v16, v87, v16
	v_fma_f32 v97, v97, s20, -v236
	v_exp_f32_e32 v86, v243
	v_add_f32_e32 v16, v82, v16
	v_exp_f32_e32 v88, v97
	v_add_f32_e32 v16, v85, v16
	v_sub_f32_e32 v2, v2, v236
	v_add_f32_e32 v16, v17, v16
	v_exp_f32_e32 v2, v2
	v_add_f32_e32 v16, v83, v16
	v_add_f32_e32 v16, v86, v16
	v_add_f32_e32 v16, v88, v16
	v_mov_b32_e32 v97, v16
	v_cmp_neq_f32_e32 vcc, 1.0, v2
	s_nop 0
	v_permlane32_swap_b32_e32 v16, v97
	s_cbranch_vccz .LBB0_1040
	v_pk_mul_f32 v[80:81], v[80:81], v[2:3] op_sel_hi:[1,0]
	v_pk_mul_f32 v[78:79], v[78:79], v[2:3] op_sel_hi:[1,0]
	v_pk_mul_f32 v[76:77], v[76:77], v[2:3] op_sel_hi:[1,0]
	v_pk_mul_f32 v[74:75], v[74:75], v[2:3] op_sel_hi:[1,0]
	v_pk_mul_f32 v[72:73], v[72:73], v[2:3] op_sel_hi:[1,0]
	v_pk_mul_f32 v[70:71], v[70:71], v[2:3] op_sel_hi:[1,0]
	v_pk_mul_f32 v[68:69], v[68:69], v[2:3] op_sel_hi:[1,0]
	v_pk_mul_f32 v[66:67], v[66:67], v[2:3] op_sel_hi:[1,0]
	v_pk_mul_f32 v[64:65], v[64:65], v[2:3] op_sel_hi:[1,0]
	v_pk_mul_f32 v[62:63], v[62:63], v[2:3] op_sel_hi:[1,0]
	v_pk_mul_f32 v[60:61], v[60:61], v[2:3] op_sel_hi:[1,0]
	v_pk_mul_f32 v[58:59], v[58:59], v[2:3] op_sel_hi:[1,0]
	v_pk_mul_f32 v[56:57], v[56:57], v[2:3] op_sel_hi:[1,0]
	v_pk_mul_f32 v[54:55], v[54:55], v[2:3] op_sel_hi:[1,0]
	v_pk_mul_f32 v[52:53], v[52:53], v[2:3] op_sel_hi:[1,0]
	v_pk_mul_f32 v[50:51], v[50:51], v[2:3] op_sel_hi:[1,0]
	v_pk_mul_f32 v[48:49], v[48:49], v[2:3] op_sel_hi:[1,0]
	v_pk_mul_f32 v[46:47], v[46:47], v[2:3] op_sel_hi:[1,0]
	v_pk_mul_f32 v[44:45], v[44:45], v[2:3] op_sel_hi:[1,0]
	v_pk_mul_f32 v[42:43], v[42:43], v[2:3] op_sel_hi:[1,0]
	v_pk_mul_f32 v[40:41], v[40:41], v[2:3] op_sel_hi:[1,0]
	v_pk_mul_f32 v[38:39], v[38:39], v[2:3] op_sel_hi:[1,0]
	v_pk_mul_f32 v[36:37], v[36:37], v[2:3] op_sel_hi:[1,0]
	v_pk_mul_f32 v[34:35], v[34:35], v[2:3] op_sel_hi:[1,0]
	v_pk_mul_f32 v[32:33], v[32:33], v[2:3] op_sel_hi:[1,0]
	v_pk_mul_f32 v[30:31], v[30:31], v[2:3] op_sel_hi:[1,0]
	v_pk_mul_f32 v[28:29], v[28:29], v[2:3] op_sel_hi:[1,0]
	v_pk_mul_f32 v[26:27], v[26:27], v[2:3] op_sel_hi:[1,0]
	v_pk_mul_f32 v[24:25], v[24:25], v[2:3] op_sel_hi:[1,0]
	v_pk_mul_f32 v[22:23], v[22:23], v[2:3] op_sel_hi:[1,0]
	v_pk_mul_f32 v[20:21], v[20:21], v[2:3] op_sel_hi:[1,0]
	v_pk_mul_f32 v[18:19], v[18:19], v[2:3] op_sel_hi:[1,0]
.LBB0_1040:
	s_add_i32 s23, s18, s23
	v_add_f32_e32 v16, v16, v16
	v_fmac_f32_e32 v16, v237, v2
	v_add3_u32 v2, s23, v229, v179
	v_add_u32_e32 v239, 0x6000, v2
	v_add_u32_e32 v237, 0x7000, v2
	v_add_u32_e32 v238, 0x8800, v2
	v_add_u32_e32 v2, 0x9800, v2
	ds_read2_b64 v[240:243], v239 offset0:128 offset1:130
	v_cvt_pk_bf16_f32 v94, v94, v96
	v_cvt_pk_bf16_f32 v95, v92, v95
	v_cvt_pk_bf16_f32 v96, v90, v93
	v_cvt_pk_bf16_f32 v97, v89, v91
	v_cvt_pk_bf16_f32 v90, v84, v87
	v_cvt_pk_bf16_f32 v91, v82, v85
	v_cvt_pk_bf16_f32 v92, v17, v83
	v_cvt_pk_bf16_f32 v93, v86, v88
	ds_read2_b64 v[82:85], v237 offset0:192 offset1:194
	ds_read2_b64 v[86:89], v238 offset1:2
	s_add_i32 s22, s22, 1
	s_bitcmp1_b32 s22, 0
	s_cselect_b32 s23, 0xac00, 0
	s_add_i32 s23, s23, 0
	s_waitcnt lgkmcnt(2)
	v_mfma_f32_32x32x16_bf16 v[66:81], v[240:243], v[94:97], v[66:81]
	ds_read2_b64 v[240:243], v2 offset0:64 offset1:66
	v_lshl_add_u64 v[208:209], v[208:209], 0, s[10:11]
	s_waitcnt lgkmcnt(2)
	v_mfma_f32_32x32x16_bf16 v[50:65], v[82:85], v[94:97], v[50:65]
	ds_read2_b64 v[82:85], v239 offset0:132 offset1:134
	v_lshl_add_u64 v[210:211], v[210:211], 0, s[12:13]
	v_lshl_add_u64 v[212:213], v[212:213], 0, s[12:13]
	s_waitcnt lgkmcnt(2)
	v_mfma_f32_32x32x16_bf16 v[34:49], v[86:89], v[94:97], v[34:49]
	ds_read2_b64 v[86:89], v237 offset0:196 offset1:198
	v_lshl_add_u64 v[214:215], v[214:215], 0, s[10:11]
	v_lshl_add_u64 v[216:217], v[216:217], 0, s[10:11]
	s_waitcnt lgkmcnt(2)
	v_mfma_f32_32x32x16_bf16 v[18:33], v[240:243], v[94:97], v[18:33]
	ds_read2_b64 v[240:243], v238 offset0:4 offset1:6
	s_waitcnt lgkmcnt(2)
	v_mfma_f32_32x32x16_bf16 v[66:81], v[82:85], v[90:93], v[66:81]
	ds_read2_b64 v[82:85], v2 offset0:68 offset1:70
	s_cmp_eq_u32 s22, 35
	s_waitcnt lgkmcnt(2)
	v_mfma_f32_32x32x16_bf16 v[50:65], v[86:89], v[90:93], v[50:65]
	s_waitcnt lgkmcnt(1)
	v_mfma_f32_32x32x16_bf16 v[34:49], v[240:243], v[90:93], v[34:49]
	s_waitcnt lgkmcnt(0)
	v_mfma_f32_32x32x16_bf16 v[18:33], v[82:85], v[90:93], v[18:33]
	v_add3_u32 v2, s23, v176, v181
	s_waitcnt vmcnt(4)
	ds_write_b128 v2, v[150:153]
	v_add3_u32 v2, s23, v222, v223
	s_waitcnt vmcnt(3)
	ds_write_b128 v2, v[146:149]
	v_add3_u32 v2, s23, v224, v225
	s_waitcnt vmcnt(2)
	ds_write_b128 v2, v[12:15]
	v_add_u32_e32 v2, s23, v226
	s_waitcnt vmcnt(1)
	ds_write_b128 v2, v[248:251] offset:25600
	v_add_u32_e32 v2, s23, v227
	s_waitcnt vmcnt(0)
	ds_write_b128 v2, v[252:255] offset:25600
	s_waitcnt lgkmcnt(0)
	s_barrier
	s_cbranch_scc1 .LBB0_1042
	v_mov_b32_e32 v237, v16
	s_branch .LBB0_1038

.LBB0_3206:
	s_bitcmp1_b32 s23, 0
	s_cselect_b32 s24, 0xac00, 0
	s_add_i32 s24, s24, 0
	v_lshl_add_u64 v[222:223], s[26:27], 0, v[190:191]
	v_lshl_add_u64 v[224:225], s[26:27], 0, v[198:199]
	v_lshl_add_u64 v[226:227], s[26:27], 0, v[196:197]
	v_lshl_add_u64 v[228:229], s[26:27], 0, v[192:193]
	v_lshl_add_u64 v[248:249], s[26:27], 0, v[194:195]
	s_waitcnt vmcnt(0)
	global_load_dwordx4 v[146:149], v[222:223], off
	global_load_dwordx4 v[142:145], v[224:225], off
	global_load_dwordx4 v[138:141], v[226:227], off
	global_load_dwordx4 v[134:137], v[228:229], off
	global_load_dwordx4 v[130:133], v[248:249], off
	v_add3_u32 v231, s24, v209, v152
	ds_read_b128 v[222:225], v231
	ds_read_b128 v[226:229], v231 offset:32
	ds_read_b128 v[248:251], v231 offset:64
	ds_read_b128 v[252:255], v231 offset:96
	v_mov_b32_e32 v189, v187
	v_max_f32_e32 v187, v189, v189
	s_waitcnt lgkmcnt(3)
	v_mfma_f32_32x32x16_bf16 v[66:81], v[222:225], v[126:129], 0
	ds_read_b128 v[222:225], v231 offset:128
	s_waitcnt lgkmcnt(3)
	v_mfma_f32_32x32x16_bf16 v[66:81], v[226:229], v[106:109], v[66:81]
	ds_read_b128 v[226:229], v231 offset:160
	s_waitcnt lgkmcnt(3)
	v_mfma_f32_32x32x16_bf16 v[66:81], v[248:251], v[102:105], v[66:81]
	ds_read_b128 v[248:251], v231 offset:192
	s_waitcnt lgkmcnt(3)
	v_mfma_f32_32x32x16_bf16 v[66:81], v[252:255], v[98:101], v[66:81]
	ds_read_b128 v[252:255], v231 offset:224
	s_waitcnt lgkmcnt(3)
	v_mfma_f32_32x32x16_bf16 v[66:81], v[222:225], v[94:97], v[66:81]
	ds_read_b128 v[222:225], v231 offset:256
	s_waitcnt lgkmcnt(3)
	v_mfma_f32_32x32x16_bf16 v[66:81], v[226:229], v[90:93], v[66:81]
	ds_read_b128 v[226:229], v231 offset:288
	s_waitcnt lgkmcnt(3)
	v_mfma_f32_32x32x16_bf16 v[66:81], v[248:251], v[86:89], v[66:81]
	ds_read_b128 v[248:251], v231 offset:320
	s_waitcnt lgkmcnt(3)
	v_mfma_f32_32x32x16_bf16 v[66:81], v[252:255], v[122:125], v[66:81]
	ds_read_b128 v[252:255], v231 offset:352
	s_waitcnt lgkmcnt(3)
	v_mfma_f32_32x32x16_bf16 v[66:81], v[222:225], v[118:121], v[66:81]
	s_waitcnt lgkmcnt(2)
	v_mfma_f32_32x32x16_bf16 v[66:81], v[226:229], v[114:117], v[66:81]
	s_waitcnt lgkmcnt(1)
	v_mfma_f32_32x32x16_bf16 v[66:81], v[248:251], v[110:113], v[66:81]
	s_waitcnt lgkmcnt(0)
	v_mfma_f32_32x32x16_bf16 v[66:81], v[252:255], v[82:85], v[66:81]
	s_nop 11
	v_max3_f32 v222, v66, s16, v67
	v_max3_f32 v222, v222, v68, v69
	v_max3_f32 v222, v222, v70, v71
	v_max3_f32 v222, v222, v72, v73
	v_max3_f32 v222, v222, v74, v75
	v_max3_f32 v222, v222, v76, v77
	v_max3_f32 v222, v222, v78, v79
	v_max3_f32 v222, v222, v80, v81
	v_mov_b32_e32 v223, v222
	s_nop 1
	v_permlane32_swap_b32_e32 v222, v223
	v_mul_f32_e32 v222, 0x3dd53b95, v222
	v_max_f32_e32 v187, v187, v222
	v_fma_f32 v66, v66, s17, -v187
	v_fma_f32 v67, v67, s17, -v187
	v_fma_f32 v229, v81, s17, -v187
	v_exp_f32_e32 v81, v66
	v_fma_f32 v68, v68, s17, -v187
	v_exp_f32_e32 v222, v67
	v_fma_f32 v69, v69, s17, -v187
	v_fma_f32 v227, v79, s17, -v187
	v_exp_f32_e32 v79, v68
	v_sub_f32_e32 v223, v189, v187
	v_fma_f32 v70, v70, s17, -v187
	v_fma_f32 v73, v73, s17, -v187
	v_fma_f32 v75, v75, s17, -v187
	v_exp_f32_e32 v189, v69
	v_fma_f32 v71, v71, s17, -v187
	v_fma_f32 v225, v77, s17, -v187
	v_fma_f32 v226, v78, s17, -v187
	v_exp_f32_e32 v77, v70
	v_exp_f32_e32 v78, v73
	v_exp_f32_e32 v73, v75
	v_add_f32_e32 v75, 0, v81
	v_fma_f32 v72, v72, s17, -v187
	v_fma_f32 v228, v80, s17, -v187
	v_exp_f32_e32 v80, v71
	v_add_f32_e32 v75, v222, v75
	v_fma_f32 v224, v76, s17, -v187
	v_exp_f32_e32 v76, v72
	v_add_f32_e32 v75, v79, v75
	v_fma_f32 v74, v74, s17, -v187
	v_add_f32_e32 v75, v189, v75
	v_exp_f32_e32 v70, v74
	v_add_f32_e32 v75, v77, v75
	v_add_f32_e32 v75, v80, v75
	v_exp_f32_e32 v68, v224
	v_add_f32_e32 v75, v76, v75
	v_exp_f32_e32 v71, v225
	v_add_f32_e32 v75, v78, v75
	v_exp_f32_e32 v67, v226
	v_add_f32_e32 v75, v70, v75
	v_exp_f32_e32 v69, v227
	v_add_f32_e32 v75, v73, v75
	v_exp_f32_e32 v72, v228
	v_add_f32_e32 v75, v68, v75
	v_exp_f32_e32 v74, v229
	v_add_f32_e32 v75, v71, v75
	v_add_f32_e32 v75, v67, v75
	v_exp_f32_e32 v66, v223
	v_add_f32_e32 v75, v69, v75
	v_add_f32_e32 v75, v72, v75
	v_add_f32_e32 v75, v74, v75
	v_mov_b32_e32 v223, v75
	v_cmp_neq_f32_e32 vcc, 1.0, v66
	s_nop 0
	v_permlane32_swap_b32_e32 v75, v223
	s_cbranch_vccz .LBB0_3208
	v_pk_mul_f32 v[64:65], v[64:65], v[66:67] op_sel_hi:[1,0]
	v_pk_mul_f32 v[62:63], v[62:63], v[66:67] op_sel_hi:[1,0]
	v_pk_mul_f32 v[60:61], v[60:61], v[66:67] op_sel_hi:[1,0]
	v_pk_mul_f32 v[58:59], v[58:59], v[66:67] op_sel_hi:[1,0]
	v_pk_mul_f32 v[56:57], v[56:57], v[66:67] op_sel_hi:[1,0]
	v_pk_mul_f32 v[54:55], v[54:55], v[66:67] op_sel_hi:[1,0]
	v_pk_mul_f32 v[52:53], v[52:53], v[66:67] op_sel_hi:[1,0]
	v_pk_mul_f32 v[50:51], v[50:51], v[66:67] op_sel_hi:[1,0]
	v_pk_mul_f32 v[48:49], v[48:49], v[66:67] op_sel_hi:[1,0]
	v_pk_mul_f32 v[46:47], v[46:47], v[66:67] op_sel_hi:[1,0]
	v_pk_mul_f32 v[44:45], v[44:45], v[66:67] op_sel_hi:[1,0]
	v_pk_mul_f32 v[42:43], v[42:43], v[66:67] op_sel_hi:[1,0]
	v_pk_mul_f32 v[40:41], v[40:41], v[66:67] op_sel_hi:[1,0]
	v_pk_mul_f32 v[38:39], v[38:39], v[66:67] op_sel_hi:[1,0]
	v_pk_mul_f32 v[36:37], v[36:37], v[66:67] op_sel_hi:[1,0]
	v_pk_mul_f32 v[34:35], v[34:35], v[66:67] op_sel_hi:[1,0]
	v_pk_mul_f32 v[32:33], v[32:33], v[66:67] op_sel_hi:[1,0]
	v_pk_mul_f32 v[30:31], v[30:31], v[66:67] op_sel_hi:[1,0]
	v_pk_mul_f32 v[28:29], v[28:29], v[66:67] op_sel_hi:[1,0]
	v_pk_mul_f32 v[26:27], v[26:27], v[66:67] op_sel_hi:[1,0]
	v_pk_mul_f32 v[24:25], v[24:25], v[66:67] op_sel_hi:[1,0]
	v_pk_mul_f32 v[22:23], v[22:23], v[66:67] op_sel_hi:[1,0]
	v_pk_mul_f32 v[20:21], v[20:21], v[66:67] op_sel_hi:[1,0]
	v_pk_mul_f32 v[18:19], v[18:19], v[66:67] op_sel_hi:[1,0]
	v_pk_mul_f32 v[16:17], v[16:17], v[66:67] op_sel_hi:[1,0]
	v_pk_mul_f32 v[14:15], v[14:15], v[66:67] op_sel_hi:[1,0]
	v_pk_mul_f32 v[12:13], v[12:13], v[66:67] op_sel_hi:[1,0]
	v_pk_mul_f32 v[10:11], v[10:11], v[66:67] op_sel_hi:[1,0]
	v_pk_mul_f32 v[8:9], v[8:9], v[66:67] op_sel_hi:[1,0]
	v_pk_mul_f32 v[6:7], v[6:7], v[66:67] op_sel_hi:[1,0]
	v_pk_mul_f32 v[4:5], v[4:5], v[66:67] op_sel_hi:[1,0]
	v_pk_mul_f32 v[2:3], v[2:3], v[66:67] op_sel_hi:[1,0]
